# v32 + pj K-loop: trailing barrier of each MFMA section moved up 2 MFMAs
# baseline (speedup 1.0000x reference)
; #define PG8_STAGE(bufoff, gbase, voff) do { _Pragma("unroll") for (int _i = 0; _i < 2; ++_i) \
;         __builtin_amdgcn_global_load_lds((const unsigned*)((const char*)(gbase) + (voff)[_i]), (LAS unsigned*)(lds + (bufoff) + ldsw + _i * 8192), 16, 0, 0); } while (0)
; #define PG8_LDA(dst, b, h) do { _Pragma("unroll") for (int m = 0; m < 4; ++m) _Pragma("unroll") for (int k = 0; k < 2; ++k) dst[m][k] = *(const LAS bf16x8*)(lds + PG8_SA(b, h) + aoff + m * 2048 + k * 1024); } while (0)
; #define PG8_LDB(dst, b, h) do { _Pragma("unroll") for (int n = 0; n < 2; ++n) _Pragma("unroll") for (int k = 0; k < 2; ++k) dst[n][k] = *(const LAS bf16x8*)(lds + PG8_SB(b, h) + boff + n * 2048 + k * 1024); } while (0)
; #define PG8_MMA(ai, bj, At, Bt) do { __builtin_amdgcn_s_setprio(1); _Pragma("unroll") for (int m = 0; m < 4; ++m) _Pragma("unroll") for (int n = 0; n < 2; ++n) _Pragma("unroll") for (int k = 0; k < 2; ++k) \
;         acc[ai][bj][m][n] = __builtin_amdgcn_mfma_f32_16x16x32_bf16(Bt[n][k], At[m][k], acc[ai][bj][m][n], 0, 0, 0); __builtin_amdgcn_s_setprio(0); } while (0)
; #define PG8_WAIT_V(n) asm volatile("s_waitcnt vmcnt(" #n ")" ::: "memory")
; #define PG8_WAIT_L(n) asm volatile("s_waitcnt lgkmcnt(" #n ")" ::: "memory")
; #define PG8_BAR __builtin_amdgcn_s_barrier()
; #define PG8_SCHED __builtin_amdgcn_sched_barrier(0)
; #define PG8_STAGE(bufoff, gbase, voff) do { _Pragma("unroll") for (int _i = 0; _i < 2; ++_i) \
;         __builtin_amdgcn_global_load_lds((const unsigned*)((const char*)(gbase) + (voff)[_i]), (LAS unsigned*)(lds + (bufoff) + ldsw + _i * 8192), 16, 0, 0); } while (0)
; #define PG8_LDA(dst, b, h) do { _Pragma("unroll") for (int m = 0; m < 4; ++m) _Pragma("unroll") for (int k = 0; k < 2; ++k) dst[m][k] = *(const LAS bf16x8*)(lds + PG8_SA(b, h) + aoff + m * 2048 + k * 1024); } while (0)
;     ...
;             PG8_LDB(B0, 0, 0); PG8_LDB(B1, 0, 1); PG8_SCHED; PG8_LDA(At, 0, 0); PG8_STAGE(PG8_SA(1, 1), a1 + hstepA, voffA);
;             PG8_WAIT_V(8); PG8_WAIT_L(0); PG8_BAR; PG8_MMA(0, 0, At, B0); PG8_MMA(0, 1, At, B1); PG8_BAR; PG8_SCHED;
;             PG8_LDA(At, 0, 1); PG8_STAGE(PG8_SB(0, 0), b2, voffB); PG8_STAGE(PG8_SB(0, 1), b2 + hstep, voffB); PG8_STAGE(PG8_SA(0, 0), a2, voffA);
;             PG8_WAIT_V(8); PG8_WAIT_L(0); PG8_BAR; if (hi_on) { PG8_MMA(1, 0, At, B0); PG8_MMA(1, 1, At, B1); } PG8_BAR; PG8_SCHED;
.LBB0_213:
	s_add_u32 s22, s6, 0xfffc0080
	s_addc_u32 s23, s7, -1
	s_add_i32 s27, 0, 0x10000
	s_cmp_eq_u32 s26, 12
	s_cselect_b32 s25, s19, s23
	s_cselect_b32 s24, s18, s22
	v_add_u32_e32 v52, s27, v1
	s_cselect_b32 s23, s21, s17
	s_cselect_b32 s22, s20, s15
	s_add_i32 s42, 0, 0x14000
	ds_read_b128 v[62:65], v52
	ds_read_b128 v[66:69], v52 offset:1024
	ds_read_b128 v[156:159], v52 offset:2048
	ds_read_b128 v[160:163], v52 offset:3072
	v_add_u32_e32 v52, s42, v1
	ds_read_b128 v[168:171], v52
	ds_read_b128 v[172:175], v52 offset:1024
	ds_read_b128 v[176:179], v52 offset:2048
	ds_read_b128 v[180:183], v52 offset:3072
	v_lshl_add_u64 v[52:53], s[6:7], 0, v[152:153]
	s_add_i32 m0, s30, 0xc000
	ds_read_b128 v[184:187], v166
	ds_read_b128 v[188:191], v166 offset:1024
	ds_read_b128 v[192:195], v166 offset:2048
	ds_read_b128 v[204:207], v166 offset:3072
	ds_read_b128 v[208:211], v166 offset:4096
	ds_read_b128 v[212:215], v166 offset:5120
	ds_read_b128 v[216:219], v166 offset:6144
	ds_read_b128 v[220:223], v166 offset:7168
	global_load_lds_dwordx4 v[52:53], off
	v_lshl_add_u64 v[52:53], s[6:7], 0, v[154:155]
	s_add_i32 m0, s30, 0xe000
	s_nop 0
	global_load_lds_dwordx4 v[52:53], off
	s_waitcnt vmcnt(8)
	s_waitcnt lgkmcnt(0)
	s_barrier
	s_setprio 1
	s_waitcnt lgkmcnt(0)
	v_mfma_f32_16x16x32_bf16 v[138:141], v[62:65], v[184:187], v[138:141]
	v_mfma_f32_16x16x32_bf16 v[134:137], v[156:159], v[184:187], v[134:137]
	v_mfma_f32_16x16x32_bf16 v[122:125], v[62:65], v[192:195], v[122:125]
	v_mfma_f32_16x16x32_bf16 v[118:121], v[156:159], v[192:195], v[118:121]
	v_mfma_f32_16x16x32_bf16 v[106:109], v[62:65], v[208:211], v[106:109]
	v_mfma_f32_16x16x32_bf16 v[102:105], v[156:159], v[208:211], v[102:105]
	v_mfma_f32_16x16x32_bf16 v[90:93], v[62:65], v[216:219], v[90:93]
	v_mfma_f32_16x16x32_bf16 v[86:89], v[156:159], v[216:219], v[86:89]
	v_mfma_f32_16x16x32_bf16 v[138:141], v[66:69], v[188:191], v[138:141]
	v_mfma_f32_16x16x32_bf16 v[134:137], v[160:163], v[188:191], v[134:137]
	v_mfma_f32_16x16x32_bf16 v[122:125], v[66:69], v[204:207], v[122:125]
	v_mfma_f32_16x16x32_bf16 v[118:121], v[160:163], v[204:207], v[118:121]
	v_mfma_f32_16x16x32_bf16 v[106:109], v[66:69], v[212:215], v[106:109]
	v_mfma_f32_16x16x32_bf16 v[102:105], v[160:163], v[212:215], v[102:105]
	v_mfma_f32_16x16x32_bf16 v[90:93], v[66:69], v[220:223], v[90:93]
	v_mfma_f32_16x16x32_bf16 v[86:89], v[160:163], v[220:223], v[86:89]
	s_setprio 0
	s_setprio 1
	v_mfma_f32_16x16x32_bf16 v[130:133], v[168:171], v[184:187], v[130:133]
	v_mfma_f32_16x16x32_bf16 v[126:129], v[176:179], v[184:187], v[126:129]
	v_mfma_f32_16x16x32_bf16 v[114:117], v[168:171], v[192:195], v[114:117]
	v_mfma_f32_16x16x32_bf16 v[110:113], v[176:179], v[192:195], v[110:113]
	v_mfma_f32_16x16x32_bf16 v[98:101], v[168:171], v[208:211], v[98:101]
	v_mfma_f32_16x16x32_bf16 v[94:97], v[176:179], v[208:211], v[94:97]
	v_mfma_f32_16x16x32_bf16 v[82:85], v[168:171], v[216:219], v[82:85]
	v_mfma_f32_16x16x32_bf16 v[78:81], v[176:179], v[216:219], v[78:81]
	v_mfma_f32_16x16x32_bf16 v[130:133], v[172:175], v[188:191], v[130:133]
	v_mfma_f32_16x16x32_bf16 v[126:129], v[180:183], v[188:191], v[126:129]
	v_mfma_f32_16x16x32_bf16 v[114:117], v[172:175], v[204:207], v[114:117]
	v_mfma_f32_16x16x32_bf16 v[110:113], v[180:183], v[204:207], v[110:113]
	v_mfma_f32_16x16x32_bf16 v[98:101], v[172:175], v[212:215], v[98:101]
	v_mfma_f32_16x16x32_bf16 v[94:97], v[180:183], v[212:215], v[94:97]
	s_barrier
	v_mfma_f32_16x16x32_bf16 v[82:85], v[172:175], v[220:223], v[82:85]
	v_mfma_f32_16x16x32_bf16 v[78:81], v[180:183], v[220:223], v[78:81]
	s_setprio 0
	s_add_i32 s27, s27, s29
	v_lshl_add_u64 v[196:197], s[22:23], 0, v[144:145]
	s_mov_b32 m0, s27
	ds_read_b128 v[184:187], v166 offset:16384
	ds_read_b128 v[188:191], v166 offset:17408
	ds_read_b128 v[192:195], v166 offset:18432
	ds_read_b128 v[204:207], v166 offset:19456
	ds_read_b128 v[208:211], v166 offset:20480
	ds_read_b128 v[212:215], v166 offset:21504
	ds_read_b128 v[216:219], v166 offset:22528
	ds_read_b128 v[220:223], v166 offset:23552
	global_load_lds_dwordx4 v[196:197], off
	s_add_i32 m0, s27, 0x2000
	s_add_u32 s36, s22, 0x40000
	v_lshl_add_u64 v[224:225], s[22:23], 0, v[148:149]
	s_addc_u32 s37, s23, 0
	s_add_i32 s27, s42, s29
	global_load_lds_dwordx4 v[224:225], off
	v_lshl_add_u64 v[52:53], s[36:37], 0, v[144:145]
	s_mov_b32 m0, s27
	v_lshl_add_u64 v[226:227], s[24:25], 0, v[142:143]
	global_load_lds_dwordx4 v[52:53], off
	v_lshl_add_u64 v[52:53], s[36:37], 0, v[148:149]
	s_add_i32 m0, s27, 0x2000
	v_lshl_add_u64 v[228:229], s[24:25], 0, v[146:147]
	global_load_lds_dwordx4 v[52:53], off
	s_mov_b32 m0, s30
	s_nop 0
	global_load_lds_dwordx4 v[226:227], off
	s_mov_b32 m0, s31
	s_nop 0
	global_load_lds_dwordx4 v[228:229], off
	s_waitcnt vmcnt(8)
	s_waitcnt lgkmcnt(0)
	s_barrier
; #define PG8_STAGE(bufoff, gbase, voff) do { _Pragma("unroll") for (int _i = 0; _i < 2; ++_i) \
;         __builtin_amdgcn_global_load_lds((const unsigned*)((const char*)(gbase) + (voff)[_i]), (LAS unsigned*)(lds + (bufoff) + ldsw + _i * 8192), 16, 0, 0); } while (0)
; #define PG8_LDA(dst, b, h) do { _Pragma("unroll") for (int m = 0; m < 4; ++m) _Pragma("unroll") for (int k = 0; k < 2; ++k) dst[m][k] = *(const LAS bf16x8*)(lds + PG8_SA(b, h) + aoff + m * 2048 + k * 1024); } while (0)
; #define PG8_LDB(dst, b, h) do { _Pragma("unroll") for (int n = 0; n < 2; ++n) _Pragma("unroll") for (int k = 0; k < 2; ++k) dst[n][k] = *(const LAS bf16x8*)(lds + PG8_SB(b, h) + boff + n * 2048 + k * 1024); } while (0)
; #define PG8_MMA(ai, bj, At, Bt) do { __builtin_amdgcn_s_setprio(1); _Pragma("unroll") for (int m = 0; m < 4; ++m) _Pragma("unroll") for (int n = 0; n < 2; ++n) _Pragma("unroll") for (int k = 0; k < 2; ++k) \
;         acc[ai][bj][m][n] = __builtin_amdgcn_mfma_f32_16x16x32_bf16(Bt[n][k], At[m][k], acc[ai][bj][m][n], 0, 0, 0); __builtin_amdgcn_s_setprio(0); } while (0)
; #define PG8_WAIT_V(n) asm volatile("s_waitcnt vmcnt(" #n ")" ::: "memory")
; #define PG8_WAIT_L(n) asm volatile("s_waitcnt lgkmcnt(" #n ")" ::: "memory")
; #define PG8_BAR __builtin_amdgcn_s_barrier()
; #define PG8_SCHED __builtin_amdgcn_sched_barrier(0)
; #define PG8_STAGE(bufoff, gbase, voff) do { _Pragma("unroll") for (int _i = 0; _i < 2; ++_i) \
;         __builtin_amdgcn_global_load_lds((const unsigned*)((const char*)(gbase) + (voff)[_i]), (LAS unsigned*)(lds + (bufoff) + ldsw + _i * 8192), 16, 0, 0); } while (0)
; #define PG8_LDA(dst, b, h) do { _Pragma("unroll") for (int m = 0; m < 4; ++m) _Pragma("unroll") for (int k = 0; k < 2; ++k) dst[m][k] = *(const LAS bf16x8*)(lds + PG8_SA(b, h) + aoff + m * 2048 + k * 1024); } while (0)
;     ...
;             PG8_LDA(At, 0, 1); PG8_STAGE(PG8_SB(0, 0), b2, voffB); PG8_STAGE(PG8_SB(0, 1), b2 + hstep, voffB); PG8_STAGE(PG8_SA(0, 0), a2, voffA);
;             PG8_WAIT_V(8); PG8_WAIT_L(0); PG8_BAR; if (hi_on) { PG8_MMA(1, 0, At, B0); PG8_MMA(1, 1, At, B1); } PG8_BAR; PG8_SCHED;
;             PG8_LDB(B0, 1, 0); PG8_LDB(B1, 1, 1); PG8_SCHED; PG8_LDA(At, 1, 0); PG8_STAGE(PG8_SA(0, 1), a2 + hstepA, voffA);
;             PG8_WAIT_V(8); PG8_WAIT_L(0); PG8_BAR; PG8_MMA(0, 0, At, B0); PG8_MMA(0, 1, At, B1); PG8_BAR; PG8_SCHED;
	s_setprio 1
	s_waitcnt lgkmcnt(0)
	v_mfma_f32_16x16x32_bf16 v[74:77], v[62:65], v[184:187], v[74:77]
	v_mfma_f32_16x16x32_bf16 v[70:73], v[156:159], v[184:187], v[70:73]
	v_mfma_f32_16x16x32_bf16 v[48:51], v[62:65], v[192:195], v[48:51]
	v_mfma_f32_16x16x32_bf16 v[44:47], v[156:159], v[192:195], v[44:47]
	v_mfma_f32_16x16x32_bf16 v[30:33], v[62:65], v[208:211], v[30:33]
	v_mfma_f32_16x16x32_bf16 v[26:29], v[156:159], v[208:211], v[26:29]
	v_mfma_f32_16x16x32_bf16 v[14:17], v[62:65], v[216:219], v[14:17]
	v_mfma_f32_16x16x32_bf16 v[10:13], v[156:159], v[216:219], v[10:13]
	v_mfma_f32_16x16x32_bf16 v[74:77], v[66:69], v[188:191], v[74:77]
	v_mfma_f32_16x16x32_bf16 v[70:73], v[160:163], v[188:191], v[70:73]
	v_mfma_f32_16x16x32_bf16 v[48:51], v[66:69], v[204:207], v[48:51]
	v_mfma_f32_16x16x32_bf16 v[44:47], v[160:163], v[204:207], v[44:47]
	v_mfma_f32_16x16x32_bf16 v[30:33], v[66:69], v[212:215], v[30:33]
	v_mfma_f32_16x16x32_bf16 v[26:29], v[160:163], v[212:215], v[26:29]
	v_mfma_f32_16x16x32_bf16 v[14:17], v[66:69], v[220:223], v[14:17]
	v_mfma_f32_16x16x32_bf16 v[10:13], v[160:163], v[220:223], v[10:13]
	s_setprio 0
	s_setprio 1
	v_mfma_f32_16x16x32_bf16 v[58:61], v[168:171], v[184:187], v[58:61]
	v_mfma_f32_16x16x32_bf16 v[52:55], v[176:179], v[184:187], v[54:57]
	v_mfma_f32_16x16x32_bf16 v[40:43], v[168:171], v[192:195], v[40:43]
	v_mfma_f32_16x16x32_bf16 v[36:39], v[176:179], v[192:195], v[36:39]
	v_mfma_f32_16x16x32_bf16 v[22:25], v[168:171], v[208:211], v[22:25]
	v_mfma_f32_16x16x32_bf16 v[18:21], v[176:179], v[208:211], v[18:21]
	v_mfma_f32_16x16x32_bf16 v[6:9], v[168:171], v[216:219], v[6:9]
	v_mfma_f32_16x16x32_bf16 v[2:5], v[176:179], v[216:219], v[2:5]
	v_mfma_f32_16x16x32_bf16 v[58:61], v[172:175], v[188:191], v[58:61]
	v_mfma_f32_16x16x32_bf16 v[52:55], v[180:183], v[188:191], v[52:55]
	v_mfma_f32_16x16x32_bf16 v[40:43], v[172:175], v[204:207], v[40:43]
	v_mfma_f32_16x16x32_bf16 v[36:39], v[180:183], v[204:207], v[36:39]
	v_mfma_f32_16x16x32_bf16 v[22:25], v[172:175], v[212:215], v[22:25]
	v_mfma_f32_16x16x32_bf16 v[18:21], v[180:183], v[212:215], v[18:21]
	s_barrier
	v_mfma_f32_16x16x32_bf16 v[6:9], v[172:175], v[220:223], v[6:9]
	v_mfma_f32_16x16x32_bf16 v[2:5], v[180:183], v[220:223], v[2:5]
	s_setprio 0
	s_add_i32 s27, 0, 0x18000
	v_add_u32_e32 v56, s27, v1
	s_add_i32 s36, 0, 0x1c000
	ds_read_b128 v[62:65], v56
	ds_read_b128 v[66:69], v56 offset:1024
	ds_read_b128 v[156:159], v56 offset:2048
	ds_read_b128 v[160:163], v56 offset:3072
	v_add_u32_e32 v56, s36, v1
	ds_read_b128 v[168:171], v56
	ds_read_b128 v[172:175], v56 offset:1024
	ds_read_b128 v[176:179], v56 offset:2048
	ds_read_b128 v[180:183], v56 offset:3072
	s_add_u32 s24, s24, 0x40000
	s_addc_u32 s25, s25, 0
	s_mov_b32 m0, s34
	v_lshl_add_u64 v[56:57], s[24:25], 0, v[142:143]
	ds_read_b128 v[184:187], v166 offset:32768
	ds_read_b128 v[188:191], v166 offset:33792
	ds_read_b128 v[192:195], v166 offset:34816
	ds_read_b128 v[204:207], v166 offset:35840
	ds_read_b128 v[208:211], v166 offset:36864
	ds_read_b128 v[212:215], v166 offset:37888
	ds_read_b128 v[216:219], v166 offset:38912
	ds_read_b128 v[220:223], v166 offset:39936
	global_load_lds_dwordx4 v[56:57], off
	v_lshl_add_u64 v[56:57], s[24:25], 0, v[146:147]
	s_mov_b32 m0, s35
	s_nop 0
	global_load_lds_dwordx4 v[56:57], off
	s_waitcnt vmcnt(8)
	s_waitcnt lgkmcnt(0)
	s_barrier
	s_setprio 1
	s_waitcnt lgkmcnt(0)
	v_mfma_f32_16x16x32_bf16 v[138:141], v[62:65], v[184:187], v[138:141]
	v_mfma_f32_16x16x32_bf16 v[134:137], v[156:159], v[184:187], v[134:137]
	v_mfma_f32_16x16x32_bf16 v[122:125], v[62:65], v[192:195], v[122:125]
	v_mfma_f32_16x16x32_bf16 v[118:121], v[156:159], v[192:195], v[118:121]
	v_mfma_f32_16x16x32_bf16 v[106:109], v[62:65], v[208:211], v[106:109]
	v_mfma_f32_16x16x32_bf16 v[102:105], v[156:159], v[208:211], v[102:105]
	v_mfma_f32_16x16x32_bf16 v[90:93], v[62:65], v[216:219], v[90:93]
	v_mfma_f32_16x16x32_bf16 v[86:89], v[156:159], v[216:219], v[86:89]
	v_mfma_f32_16x16x32_bf16 v[138:141], v[66:69], v[188:191], v[138:141]
	v_mfma_f32_16x16x32_bf16 v[134:137], v[160:163], v[188:191], v[134:137]
	v_mfma_f32_16x16x32_bf16 v[122:125], v[66:69], v[204:207], v[122:125]
	v_mfma_f32_16x16x32_bf16 v[118:121], v[160:163], v[204:207], v[118:121]
	v_mfma_f32_16x16x32_bf16 v[106:109], v[66:69], v[212:215], v[106:109]
	v_mfma_f32_16x16x32_bf16 v[102:105], v[160:163], v[212:215], v[102:105]
	v_mfma_f32_16x16x32_bf16 v[90:93], v[66:69], v[220:223], v[90:93]
	v_mfma_f32_16x16x32_bf16 v[86:89], v[160:163], v[220:223], v[86:89]
	s_setprio 0
	s_setprio 1
	v_mfma_f32_16x16x32_bf16 v[130:133], v[168:171], v[184:187], v[130:133]
	v_mfma_f32_16x16x32_bf16 v[126:129], v[176:179], v[184:187], v[126:129]
	v_mfma_f32_16x16x32_bf16 v[114:117], v[168:171], v[192:195], v[114:117]
	v_mfma_f32_16x16x32_bf16 v[110:113], v[176:179], v[192:195], v[110:113]
	v_mfma_f32_16x16x32_bf16 v[98:101], v[168:171], v[208:211], v[98:101]
	v_mfma_f32_16x16x32_bf16 v[94:97], v[176:179], v[208:211], v[94:97]
	v_mfma_f32_16x16x32_bf16 v[82:85], v[168:171], v[216:219], v[82:85]
	v_mfma_f32_16x16x32_bf16 v[78:81], v[176:179], v[216:219], v[78:81]
	v_mfma_f32_16x16x32_bf16 v[130:133], v[172:175], v[188:191], v[130:133]
	v_mfma_f32_16x16x32_bf16 v[126:129], v[180:183], v[188:191], v[126:129]
	v_mfma_f32_16x16x32_bf16 v[114:117], v[172:175], v[204:207], v[114:117]
	v_mfma_f32_16x16x32_bf16 v[110:113], v[180:183], v[204:207], v[110:113]
	v_mfma_f32_16x16x32_bf16 v[98:101], v[172:175], v[212:215], v[98:101]
	v_mfma_f32_16x16x32_bf16 v[94:97], v[180:183], v[212:215], v[94:97]
	s_barrier
; #define PG8_STAGE(bufoff, gbase, voff) do { _Pragma("unroll") for (int _i = 0; _i < 2; ++_i) \
;         __builtin_amdgcn_global_load_lds((const unsigned*)((const char*)(gbase) + (voff)[_i]), (LAS unsigned*)(lds + (bufoff) + ldsw + _i * 8192), 16, 0, 0); } while (0)
; #define PG8_LDA(dst, b, h) do { _Pragma("unroll") for (int m = 0; m < 4; ++m) _Pragma("unroll") for (int k = 0; k < 2; ++k) dst[m][k] = *(const LAS bf16x8*)(lds + PG8_SA(b, h) + aoff + m * 2048 + k * 1024); } while (0)
; #define PG8_LDB(dst, b, h) do { _Pragma("unroll") for (int n = 0; n < 2; ++n) _Pragma("unroll") for (int k = 0; k < 2; ++k) dst[n][k] = *(const LAS bf16x8*)(lds + PG8_SB(b, h) + boff + n * 2048 + k * 1024); } while (0)
; #define PG8_MMA(ai, bj, At, Bt) do { __builtin_amdgcn_s_setprio(1); _Pragma("unroll") for (int m = 0; m < 4; ++m) _Pragma("unroll") for (int n = 0; n < 2; ++n) _Pragma("unroll") for (int k = 0; k < 2; ++k) \
;         acc[ai][bj][m][n] = __builtin_amdgcn_mfma_f32_16x16x32_bf16(Bt[n][k], At[m][k], acc[ai][bj][m][n], 0, 0, 0); __builtin_amdgcn_s_setprio(0); } while (0)
; #define PG8_WAIT_V(n) asm volatile("s_waitcnt vmcnt(" #n ")" ::: "memory")
; #define PG8_WAIT_L(n) asm volatile("s_waitcnt lgkmcnt(" #n ")" ::: "memory")
; #define PG8_BAR __builtin_amdgcn_s_barrier()
; #define PG8_SCHED __builtin_amdgcn_sched_barrier(0)
; #define PG8_STAGE(bufoff, gbase, voff) do { _Pragma("unroll") for (int _i = 0; _i < 2; ++_i) \
;         __builtin_amdgcn_global_load_lds((const unsigned*)((const char*)(gbase) + (voff)[_i]), (LAS unsigned*)(lds + (bufoff) + ldsw + _i * 8192), 16, 0, 0); } while (0)
; #define PG8_LDA(dst, b, h) do { _Pragma("unroll") for (int m = 0; m < 4; ++m) _Pragma("unroll") for (int k = 0; k < 2; ++k) dst[m][k] = *(const LAS bf16x8*)(lds + PG8_SA(b, h) + aoff + m * 2048 + k * 1024); } while (0)
;     ...
;             PG8_LDB(B0, 1, 0); PG8_LDB(B1, 1, 1); PG8_SCHED; PG8_LDA(At, 1, 0); PG8_STAGE(PG8_SA(0, 1), a2 + hstepA, voffA);
;             PG8_WAIT_V(8); PG8_WAIT_L(0); PG8_BAR; PG8_MMA(0, 0, At, B0); PG8_MMA(0, 1, At, B1); PG8_BAR; PG8_SCHED;
;             PG8_LDA(At, 1, 1); PG8_STAGE(PG8_SB(1, 0), b3, voffB); PG8_STAGE(PG8_SB(1, 1), b3 + hstep, voffB); PG8_STAGE(PG8_SA(1, 0), a3, voffA);
;             PG8_WAIT_V(8); PG8_WAIT_L(0); PG8_BAR; if (hi_on) { PG8_MMA(1, 0, At, B0); PG8_MMA(1, 1, At, B1); } PG8_BAR; PG8_SCHED;
;         }
	v_mfma_f32_16x16x32_bf16 v[82:85], v[172:175], v[220:223], v[82:85]
	v_mfma_f32_16x16x32_bf16 v[78:81], v[180:183], v[220:223], v[78:81]
	s_setprio 0
	s_add_i32 s24, s27, s29
	v_lshl_add_u64 v[56:57], v[196:197], 0, s[88:89]
	s_mov_b32 m0, s24
	ds_read_b128 v[184:187], v166 offset:49152
	ds_read_b128 v[188:191], v166 offset:50176
	ds_read_b128 v[192:195], v166 offset:51200
	ds_read_b128 v[204:207], v166 offset:52224
	ds_read_b128 v[208:211], v166 offset:53248
	ds_read_b128 v[212:215], v166 offset:54272
	ds_read_b128 v[216:219], v166 offset:55296
	ds_read_b128 v[220:223], v166 offset:56320
	global_load_lds_dwordx4 v[56:57], off
	s_add_i32 m0, s24, 0x2000
	s_add_u32 s22, s22, 0x40080
	v_lshl_add_u64 v[56:57], v[224:225], 0, s[88:89]
	s_addc_u32 s23, s23, 0
	s_add_i32 s24, s36, s29
	global_load_lds_dwordx4 v[56:57], off
	v_lshl_add_u64 v[56:57], s[22:23], 0, v[144:145]
	s_mov_b32 m0, s24
	s_nop 0
	global_load_lds_dwordx4 v[56:57], off
	v_lshl_add_u64 v[56:57], s[22:23], 0, v[148:149]
	s_add_i32 m0, s24, 0x2000
	s_nop 0
	global_load_lds_dwordx4 v[56:57], off
	v_lshl_add_u64 v[56:57], v[226:227], 0, s[88:89]
	s_mov_b32 m0, s39
	s_nop 0
	global_load_lds_dwordx4 v[56:57], off
	v_lshl_add_u64 v[56:57], v[228:229], 0, s[88:89]
	s_mov_b32 m0, s40
	s_nop 0
	global_load_lds_dwordx4 v[56:57], off
	s_waitcnt vmcnt(8)
	s_waitcnt lgkmcnt(0)
	s_barrier
	s_setprio 1
	s_waitcnt lgkmcnt(0)
	v_mfma_f32_16x16x32_bf16 v[74:77], v[62:65], v[184:187], v[74:77]
	v_mfma_f32_16x16x32_bf16 v[70:73], v[156:159], v[184:187], v[70:73]
	v_mfma_f32_16x16x32_bf16 v[48:51], v[62:65], v[192:195], v[48:51]
	v_mfma_f32_16x16x32_bf16 v[44:47], v[156:159], v[192:195], v[44:47]
	v_mfma_f32_16x16x32_bf16 v[30:33], v[62:65], v[208:211], v[30:33]
	v_mfma_f32_16x16x32_bf16 v[26:29], v[156:159], v[208:211], v[26:29]
	v_mfma_f32_16x16x32_bf16 v[14:17], v[62:65], v[216:219], v[14:17]
	v_mfma_f32_16x16x32_bf16 v[10:13], v[156:159], v[216:219], v[10:13]
	v_mfma_f32_16x16x32_bf16 v[74:77], v[66:69], v[188:191], v[74:77]
	v_mfma_f32_16x16x32_bf16 v[70:73], v[160:163], v[188:191], v[70:73]
	v_mfma_f32_16x16x32_bf16 v[48:51], v[66:69], v[204:207], v[48:51]
	v_mfma_f32_16x16x32_bf16 v[44:47], v[160:163], v[204:207], v[44:47]
	v_mfma_f32_16x16x32_bf16 v[30:33], v[66:69], v[212:215], v[30:33]
	v_mfma_f32_16x16x32_bf16 v[26:29], v[160:163], v[212:215], v[26:29]
	v_mfma_f32_16x16x32_bf16 v[14:17], v[66:69], v[220:223], v[14:17]
	v_mfma_f32_16x16x32_bf16 v[10:13], v[160:163], v[220:223], v[10:13]
	s_setprio 0
	s_setprio 1
	v_mfma_f32_16x16x32_bf16 v[56:59], v[168:171], v[184:187], v[58:61]
	v_mfma_f32_16x16x32_bf16 v[52:55], v[176:179], v[184:187], v[52:55]
	v_mfma_f32_16x16x32_bf16 v[40:43], v[168:171], v[192:195], v[40:43]
	v_mfma_f32_16x16x32_bf16 v[36:39], v[176:179], v[192:195], v[36:39]
	v_mfma_f32_16x16x32_bf16 v[22:25], v[168:171], v[208:211], v[22:25]
	v_mfma_f32_16x16x32_bf16 v[18:21], v[176:179], v[208:211], v[18:21]
	v_mfma_f32_16x16x32_bf16 v[6:9], v[168:171], v[216:219], v[6:9]
	v_mfma_f32_16x16x32_bf16 v[2:5], v[176:179], v[216:219], v[2:5]
	v_mfma_f32_16x16x32_bf16 v[58:61], v[172:175], v[188:191], v[56:59]
	v_mfma_f32_16x16x32_bf16 v[54:57], v[180:183], v[188:191], v[52:55]
	v_mfma_f32_16x16x32_bf16 v[40:43], v[172:175], v[204:207], v[40:43]
	v_mfma_f32_16x16x32_bf16 v[36:39], v[180:183], v[204:207], v[36:39]
	v_mfma_f32_16x16x32_bf16 v[22:25], v[172:175], v[212:215], v[22:25]
	v_mfma_f32_16x16x32_bf16 v[18:21], v[180:183], v[212:215], v[18:21]
	s_barrier
	v_mfma_f32_16x16x32_bf16 v[6:9], v[172:175], v[220:223], v[6:9]
	v_mfma_f32_16x16x32_bf16 v[2:5], v[180:183], v[220:223], v[2:5]
	s_setprio 0
	s_add_i32 s26, s26, 2
	s_add_u32 s6, s6, 0x100
	s_addc_u32 s7, s7, 0
	s_add_u32 s15, s15, 0x100
	s_addc_u32 s17, s17, 0
	s_cmp_gt_u32 s26, 13
	s_cbranch_scc0 .LBB0_213
	s_and_b64 vcc, exec, s[12:13]
	s_cbranch_vccz .LBB0_216
	s_barrier
